# up-GEMM epilogue: 8 hazard pads per unit replaced by moving an independent VALU op into the slot (on top of attention store widening)
# baseline (speedup 1.0000x reference)
.LBB0_1916:
	s_mov_b32 s29, 0
	v_mov_b32_e32 v4, v166
	v_mov_b32_e32 v2, v167
	v_mov_b32_e32 v3, s24
	s_add_u32 s40, s2, 0xffffff00
	ds_read_b32 v3, v3 offset:288
	s_addc_u32 s41, s23, -1
	s_lshl_b32 s2, s31, 11
	s_add_i32 s2, s2, 0
	v_lshl_add_u32 v18, v2, 3, s83
	s_add_i32 s2, s2, 0x21000
	v_lshl_add_u32 v5, v18, 3, s2
	ds_read_b128 v[14:17], v5
	s_waitcnt lgkmcnt(1)
	v_readfirstlane_b32 s8, v3
	s_lshl_b32 s8, s8, 2
	s_add_i32 s8, s8, 0
	s_add_i32 s8, s8, 0x201c0
	v_mov_b32_e32 v2, s8
	ds_read2_b32 v[2:3], v2 offset1:32
	v_add_u32_e32 v19, s82, v4
	ds_read_b128 v[10:13], v5 offset:16
	ds_read_b128 v[6:9], v5 offset:32
	v_add_u32_e32 v22, 16, v19
	v_add_u32_e32 v24, 32, v19
	s_waitcnt lgkmcnt(2)
	v_readfirstlane_b32 s9, v2
	v_lshl_add_u32 v2, v19, 2, s2
	ds_read_b32 v20, v2 offset:1024
	v_readfirstlane_b32 s8, v3
	s_sub_i32 s8, s36, s8
	v_lshl_add_u32 v23, v22, 2, s2
	v_lshl_add_u32 v25, v24, 2, s2
	s_lshl_b32 s8, s8, 8
	ds_read_b128 v[2:5], v5 offset:48
	ds_read_b32 v23, v23 offset:1024
	ds_read_b32 v25, v25 offset:1024
	v_add_u32_e32 v21, s8, v19
	s_waitcnt lgkmcnt(3)
	v_mul_f32_e32 v20, 0x3b800000, v20
	v_cmp_gt_i32_e32 vcc, s9, v21
	s_waitcnt lgkmcnt(1)
	v_mul_f32_e32 v21, 0x3b800000, v23
	v_add_u32_e32 v26, 0xa0, v19
	v_cndmask_b32_e32 v180, 0, v20, vcc
	v_add_u32_e32 v20, s8, v22
	v_cmp_gt_i32_e32 vcc, s9, v20
	v_add_u32_e32 v20, s8, v24
	v_add_u32_e32 v22, 0x80, v19
	v_cndmask_b32_e32 v164, 0, v21, vcc
	s_waitcnt lgkmcnt(0)
	v_mul_f32_e32 v21, 0x3b800000, v25
	v_cmp_gt_i32_e32 vcc, s9, v20
	v_add_u32_e32 v20, 48, v19
	v_add_u32_e32 v24, 0x90, v19
	v_cndmask_b32_e32 v162, 0, v21, vcc
	v_lshl_add_u32 v21, v20, 2, s2
	v_lshl_add_u32 v23, v22, 2, s2
	v_lshl_add_u32 v25, v24, 2, s2
	v_lshl_add_u32 v27, v26, 2, s2
	v_add_u32_e32 v29, 0xb0, v19
	v_add_u32_e32 v20, s8, v20
	v_lshl_add_u32 v28, v29, 2, s2
	ds_read_b32 v21, v21 offset:1024
	ds_read_b32 v23, v23 offset:1024
	ds_read_b32 v25, v25 offset:1024
	ds_read_b32 v27, v27 offset:1024
	ds_read_b32 v31, v28 offset:1024
	s_waitcnt lgkmcnt(4)
	v_mul_f32_e32 v21, 0x3b800000, v21
	v_cmp_gt_i32_e32 vcc, s9, v20
	v_add_u32_e32 v20, s8, v22
	s_lshl_b32 s42, s14, 7
	v_cndmask_b32_e32 v32, 0, v21, vcc
	s_waitcnt lgkmcnt(3)
	v_mul_f32_e32 v21, 0x3b800000, v23
	v_cmp_gt_i32_e32 vcc, s9, v20
	v_add_u32_e32 v20, s8, v24
	v_mov_b32_e32 v24, v14
	v_cndmask_b32_e32 v30, 0, v21, vcc
	s_waitcnt lgkmcnt(2)
	v_mul_f32_e32 v21, 0x3b800000, v25
	v_mov_b32_e32 v25, v16
	v_pk_fma_f32 v[182:183], v[158:159], v[180:181], v[24:25] op_sel_hi:[1,0,1]
	v_mov_b32_e32 v16, v15
	v_min_f32_e32 v182, 0x40e00000, v182
	v_min_f32_e32 v183, 0x40e00000, v183
	v_pk_mul_f32 v[184:185], v[182:183], s[20:21] op_sel_hi:[1,0]
	v_cmp_gt_i32_e32 vcc, s9, v20
	v_exp_f32_e32 v184, v184
	v_exp_f32_e32 v185, v185
	v_add_u32_e32 v20, s8, v26
	v_cndmask_b32_e32 v28, 0, v21, vcc
	s_waitcnt lgkmcnt(1)
	v_mul_f32_e32 v21, 0x3b800000, v27
	v_pk_add_f32 v[14:15], v[184:185], 1.0 op_sel_hi:[1,0]
	v_pk_fma_f32 v[184:185], v[126:127], v[180:181], v[16:17] op_sel_hi:[1,0,1]
	v_rcp_f32_e32 v14, v14
	v_rcp_f32_e32 v15, v15
	v_med3_f32 v184, v184, s37, v176
	v_med3_f32 v185, v185, s37, v176
	v_cmp_gt_i32_e32 vcc, s9, v20
	v_pk_mul_f32 v[14:15], v[182:183], v[14:15]
	v_add_u32_e32 v20, s8, v29
	v_pk_fma_f32 v[182:183], v[184:185], v[14:15], v[14:15]
	v_mov_b32_e32 v14, v10
	v_mov_b32_e32 v15, v12
	v_pk_fma_f32 v[184:185], v[160:161], v[180:181], v[14:15] op_sel_hi:[1,0,1]
	v_mov_b32_e32 v12, v11
	v_min_f32_e32 v184, 0x40e00000, v184
	v_min_f32_e32 v185, 0x40e00000, v185
	v_pk_mul_f32 v[186:187], v[184:185], s[20:21] op_sel_hi:[1,0]
	v_cndmask_b32_e32 v26, 0, v21, vcc
	v_exp_f32_e32 v186, v186
	v_exp_f32_e32 v187, v187
	s_waitcnt lgkmcnt(0)
	v_mul_f32_e32 v21, 0x3b800000, v31
	v_cmp_gt_i32_e32 vcc, s9, v20
	v_pk_add_f32 v[10:11], v[186:187], 1.0 op_sel_hi:[1,0]
	v_cndmask_b32_e32 v22, 0, v21, vcc
	v_rcp_f32_e32 v10, v10
	v_rcp_f32_e32 v11, v11
	v_cvt_pk_fp8_f32 v192, v182, v183
	v_pk_fma_f32 v[182:183], v[128:129], v[180:181], v[12:13] op_sel_hi:[1,0,1]
	v_pk_mul_f32 v[10:11], v[184:185], v[10:11]
	v_med3_f32 v182, v182, s37, v176
	v_med3_f32 v183, v183, s37, v176
	v_pk_fma_f32 v[182:183], v[182:183], v[10:11], v[10:11]
	v_mov_b32_e32 v10, v6
	v_mov_b32_e32 v11, v8
	v_pk_fma_f32 v[184:185], v[154:155], v[180:181], v[10:11] op_sel_hi:[1,0,1]
	v_mov_b32_e32 v8, v7
	v_min_f32_e32 v184, 0x40e00000, v184
	v_min_f32_e32 v185, 0x40e00000, v185
	v_pk_mul_f32 v[186:187], v[184:185], s[20:21] op_sel_hi:[1,0]
	v_cvt_pk_fp8_f32 v192, v182, v183 op_sel:[0,0,1]
	v_exp_f32_e32 v186, v186
	v_exp_f32_e32 v187, v187
	v_pk_fma_f32 v[182:183], v[122:123], v[180:181], v[8:9] op_sel_hi:[1,0,1]
	v_med3_f32 v182, v182, s37, v176
	v_pk_add_f32 v[6:7], v[186:187], 1.0 op_sel_hi:[1,0]
	v_med3_f32 v183, v183, s37, v176
	v_rcp_f32_e32 v6, v6
	v_rcp_f32_e32 v7, v7
	v_lshl_add_u32 v20, s36, 8, v19
	s_ashr_i32 s43, s42, 31
	v_pk_mul_f32 v[6:7], v[184:185], v[6:7]
	v_ashrrev_i32_e32 v19, 31, v18
	v_pk_fma_f32 v[182:183], v[182:183], v[6:7], v[6:7]
	v_mov_b32_e32 v6, v2
	v_mov_b32_e32 v7, v4
	v_pk_fma_f32 v[184:185], v[156:157], v[180:181], v[6:7] op_sel_hi:[1,0,1]
	v_mov_b32_e32 v4, v3
	v_min_f32_e32 v184, 0x40e00000, v184
	v_min_f32_e32 v185, 0x40e00000, v185
	v_pk_mul_f32 v[186:187], v[184:185], s[20:21] op_sel_hi:[1,0]
	v_pk_fma_f32 v[180:181], v[124:125], v[180:181], v[4:5] op_sel_hi:[1,0,1]
	v_exp_f32_e32 v186, v186
	v_exp_f32_e32 v187, v187
	v_cvt_pk_fp8_f32 v193, v182, v183
	v_med3_f32 v180, v180, s37, v176
	v_med3_f32 v181, v181, s37, v176
	v_pk_add_f32 v[2:3], v[186:187], 1.0 op_sel_hi:[1,0]
	v_pk_fma_f32 v[182:183], v[150:151], v[164:165], v[24:25] op_sel_hi:[1,0,1]
	v_rcp_f32_e32 v2, v2
	v_rcp_f32_e32 v3, v3
	v_min_f32_e32 v182, 0x40e00000, v182
	v_min_f32_e32 v183, 0x40e00000, v183
	s_and_b64 vcc, exec, s[6:7]
	v_pk_mul_f32 v[2:3], v[184:185], v[2:3]
	v_pk_mul_f32 v[184:185], v[182:183], s[20:21] op_sel_hi:[1,0]
	v_pk_fma_f32 v[2:3], v[180:181], v[2:3], v[2:3]
	v_exp_f32_e32 v184, v184
	v_cvt_pk_fp8_f32 v193, v2, v3 op_sel:[0,0,1]
	v_ashrrev_i32_e32 v21, 31, v20
	v_lshlrev_b64 v[180:181], 10, v[20:21]
	v_exp_f32_e32 v185, v185
	v_lshl_add_u64 v[180:181], s[12:13], 0, v[180:181]
	v_lshl_add_u64 v[180:181], v[180:181], 0, s[42:43]
	v_lshl_add_u64 v[188:189], v[180:181], 0, v[18:19]
	global_store_dwordx2 v[188:189], v[192:193], off
	v_pk_add_f32 v[2:3], v[184:185], 1.0 op_sel_hi:[1,0]
	v_pk_fma_f32 v[180:181], v[118:119], v[164:165], v[16:17] op_sel_hi:[1,0,1]
	v_rcp_f32_e32 v2, v2
	v_rcp_f32_e32 v3, v3
	v_med3_f32 v180, v180, s37, v176
	v_med3_f32 v181, v181, s37, v176
	v_pk_mul_f32 v[2:3], v[182:183], v[2:3]
	v_pk_fma_f32 v[182:183], v[152:153], v[164:165], v[14:15] op_sel_hi:[1,0,1]
	v_pk_fma_f32 v[2:3], v[180:181], v[2:3], v[2:3]
	v_min_f32_e32 v182, 0x40e00000, v182
	v_min_f32_e32 v183, 0x40e00000, v183
	v_pk_mul_f32 v[184:185], v[182:183], s[20:21] op_sel_hi:[1,0]
	v_cvt_pk_fp8_f32 v194, v2, v3
	v_exp_f32_e32 v184, v184
	v_exp_f32_e32 v185, v185
	v_pk_fma_f32 v[180:181], v[120:121], v[164:165], v[12:13] op_sel_hi:[1,0,1]
	v_med3_f32 v180, v180, s37, v176
	v_pk_add_f32 v[2:3], v[184:185], 1.0 op_sel_hi:[1,0]
	v_med3_f32 v181, v181, s37, v176
	v_rcp_f32_e32 v2, v2
	v_rcp_f32_e32 v3, v3
	s_nop 0
	v_pk_mul_f32 v[2:3], v[182:183], v[2:3]
	v_pk_fma_f32 v[182:183], v[146:147], v[164:165], v[10:11] op_sel_hi:[1,0,1]
	v_pk_fma_f32 v[2:3], v[180:181], v[2:3], v[2:3]
	v_min_f32_e32 v182, 0x40e00000, v182
	v_min_f32_e32 v183, 0x40e00000, v183
	v_pk_mul_f32 v[184:185], v[182:183], s[20:21] op_sel_hi:[1,0]
	v_cvt_pk_fp8_f32 v194, v2, v3 op_sel:[0,0,1]
	v_exp_f32_e32 v184, v184
	v_exp_f32_e32 v185, v185
	v_pk_fma_f32 v[180:181], v[114:115], v[164:165], v[8:9] op_sel_hi:[1,0,1]
	v_pk_add_f32 v[2:3], v[184:185], 1.0 op_sel_hi:[1,0]
	v_med3_f32 v180, v180, s37, v176
	v_rcp_f32_e32 v2, v2
	v_rcp_f32_e32 v3, v3
	v_med3_f32 v181, v181, s37, v176
	v_pk_mul_f32 v[2:3], v[182:183], v[2:3]
	v_pk_fma_f32 v[182:183], v[148:149], v[164:165], v[6:7] op_sel_hi:[1,0,1]
	v_pk_fma_f32 v[2:3], v[180:181], v[2:3], v[2:3]
	v_min_f32_e32 v182, 0x40e00000, v182
	v_min_f32_e32 v183, 0x40e00000, v183
	v_pk_mul_f32 v[184:185], v[182:183], s[20:21] op_sel_hi:[1,0]
	v_cvt_pk_fp8_f32 v195, v2, v3
	v_exp_f32_e32 v184, v184
	v_exp_f32_e32 v185, v185
	v_pk_fma_f32 v[180:181], v[116:117], v[164:165], v[4:5] op_sel_hi:[1,0,1]
	v_pk_add_f32 v[2:3], v[184:185], 1.0 op_sel_hi:[1,0]
	v_med3_f32 v180, v180, s37, v176
	v_rcp_f32_e32 v2, v2
	v_rcp_f32_e32 v3, v3
	v_med3_f32 v181, v181, s37, v176
	v_pk_mul_f32 v[2:3], v[182:183], v[2:3]
	v_pk_fma_f32 v[182:183], v[142:143], v[162:163], v[24:25] op_sel_hi:[1,0,1]
	v_pk_fma_f32 v[2:3], v[180:181], v[2:3], v[2:3]
	v_min_f32_e32 v182, 0x40e00000, v182
	v_min_f32_e32 v183, 0x40e00000, v183
	v_cvt_pk_fp8_f32 v195, v2, v3 op_sel:[0,0,1]
	v_pk_mul_f32 v[184:185], v[182:183], s[20:21] op_sel_hi:[1,0]
	v_exp_f32_e32 v184, v184
	v_exp_f32_e32 v185, v185
	s_mov_b32 s28, 0x4000
	v_lshl_add_u64 v[180:181], v[188:189], 0, s[28:29]
	global_store_dwordx2 v[180:181], v[194:195], off
	v_pk_add_f32 v[2:3], v[184:185], 1.0 op_sel_hi:[1,0]
	v_pk_fma_f32 v[180:181], v[110:111], v[162:163], v[16:17] op_sel_hi:[1,0,1]
	v_rcp_f32_e32 v2, v2
	v_rcp_f32_e32 v3, v3
	v_med3_f32 v180, v180, s37, v176
	v_med3_f32 v181, v181, s37, v176
	v_pk_mul_f32 v[2:3], v[182:183], v[2:3]
	v_pk_fma_f32 v[182:183], v[144:145], v[162:163], v[14:15] op_sel_hi:[1,0,1]
	v_pk_fma_f32 v[2:3], v[180:181], v[2:3], v[2:3]
	v_min_f32_e32 v182, 0x40e00000, v182
	v_min_f32_e32 v183, 0x40e00000, v183
	v_pk_mul_f32 v[184:185], v[182:183], s[20:21] op_sel_hi:[1,0]
	v_cvt_pk_fp8_f32 v196, v2, v3
	v_exp_f32_e32 v184, v184
	v_exp_f32_e32 v185, v185
	v_pk_fma_f32 v[180:181], v[112:113], v[162:163], v[12:13] op_sel_hi:[1,0,1]
	v_med3_f32 v180, v180, s37, v176
	v_pk_add_f32 v[2:3], v[184:185], 1.0 op_sel_hi:[1,0]
	v_med3_f32 v181, v181, s37, v176
	v_rcp_f32_e32 v2, v2
	v_rcp_f32_e32 v3, v3
	s_nop 0
	v_pk_mul_f32 v[2:3], v[182:183], v[2:3]
	v_pk_fma_f32 v[182:183], v[138:139], v[162:163], v[10:11] op_sel_hi:[1,0,1]
	v_pk_fma_f32 v[2:3], v[180:181], v[2:3], v[2:3]
	v_min_f32_e32 v182, 0x40e00000, v182
	v_min_f32_e32 v183, 0x40e00000, v183
	v_pk_mul_f32 v[184:185], v[182:183], s[20:21] op_sel_hi:[1,0]
	v_cvt_pk_fp8_f32 v196, v2, v3 op_sel:[0,0,1]
	v_exp_f32_e32 v184, v184
	v_exp_f32_e32 v185, v185
	v_pk_fma_f32 v[180:181], v[106:107], v[162:163], v[8:9] op_sel_hi:[1,0,1]
	v_pk_add_f32 v[2:3], v[184:185], 1.0 op_sel_hi:[1,0]
	v_med3_f32 v180, v180, s37, v176
	v_rcp_f32_e32 v2, v2
	v_rcp_f32_e32 v3, v3
	v_med3_f32 v181, v181, s37, v176
	v_pk_mul_f32 v[2:3], v[182:183], v[2:3]
	v_pk_fma_f32 v[182:183], v[140:141], v[162:163], v[6:7] op_sel_hi:[1,0,1]
	v_pk_fma_f32 v[2:3], v[180:181], v[2:3], v[2:3]
	v_min_f32_e32 v182, 0x40e00000, v182
	v_min_f32_e32 v183, 0x40e00000, v183
	v_pk_mul_f32 v[184:185], v[182:183], s[20:21] op_sel_hi:[1,0]
	v_cvt_pk_fp8_f32 v197, v2, v3
	v_exp_f32_e32 v184, v184
	v_exp_f32_e32 v185, v185
	v_pk_fma_f32 v[180:181], v[108:109], v[162:163], v[4:5] op_sel_hi:[1,0,1]
	v_pk_add_f32 v[2:3], v[184:185], 1.0 op_sel_hi:[1,0]
	v_med3_f32 v180, v180, s37, v176
	v_rcp_f32_e32 v2, v2
	v_rcp_f32_e32 v3, v3
	v_med3_f32 v181, v181, s37, v176
	v_pk_mul_f32 v[2:3], v[182:183], v[2:3]
	v_pk_fma_f32 v[182:183], v[134:135], v[32:33], v[24:25] op_sel_hi:[1,0,1]
	v_pk_fma_f32 v[2:3], v[180:181], v[2:3], v[2:3]
	v_min_f32_e32 v182, 0x40e00000, v182
	v_min_f32_e32 v183, 0x40e00000, v183
	v_cvt_pk_fp8_f32 v197, v2, v3 op_sel:[0,0,1]
	v_pk_mul_f32 v[184:185], v[182:183], s[20:21] op_sel_hi:[1,0]
	v_exp_f32_e32 v184, v184
	v_exp_f32_e32 v185, v185
	s_mov_b32 s28, 0x8000
	v_lshl_add_u64 v[180:181], v[188:189], 0, s[28:29]
	global_store_dwordx2 v[180:181], v[196:197], off
	v_pk_add_f32 v[2:3], v[184:185], 1.0 op_sel_hi:[1,0]
	v_pk_fma_f32 v[180:181], v[102:103], v[32:33], v[16:17] op_sel_hi:[1,0,1]
	v_rcp_f32_e32 v2, v2
	v_rcp_f32_e32 v3, v3
	v_med3_f32 v180, v180, s37, v176
	v_med3_f32 v181, v181, s37, v176
	v_pk_mul_f32 v[2:3], v[182:183], v[2:3]
	v_pk_fma_f32 v[182:183], v[136:137], v[32:33], v[14:15] op_sel_hi:[1,0,1]
	v_pk_fma_f32 v[2:3], v[180:181], v[2:3], v[2:3]
	v_min_f32_e32 v182, 0x40e00000, v182
	v_min_f32_e32 v183, 0x40e00000, v183
	v_pk_mul_f32 v[184:185], v[182:183], s[20:21] op_sel_hi:[1,0]
	v_cvt_pk_fp8_f32 v198, v2, v3
	v_exp_f32_e32 v184, v184
	v_exp_f32_e32 v185, v185
	v_pk_fma_f32 v[180:181], v[104:105], v[32:33], v[12:13] op_sel_hi:[1,0,1]
	v_med3_f32 v180, v180, s37, v176
	v_pk_add_f32 v[2:3], v[184:185], 1.0 op_sel_hi:[1,0]
	v_med3_f32 v181, v181, s37, v176
	v_rcp_f32_e32 v2, v2
	v_rcp_f32_e32 v3, v3
	s_nop 0
	v_pk_mul_f32 v[2:3], v[182:183], v[2:3]
	v_pk_fma_f32 v[182:183], v[130:131], v[32:33], v[10:11] op_sel_hi:[1,0,1]
	v_pk_fma_f32 v[2:3], v[180:181], v[2:3], v[2:3]
	v_min_f32_e32 v182, 0x40e00000, v182
	v_min_f32_e32 v183, 0x40e00000, v183
	v_pk_mul_f32 v[184:185], v[182:183], s[20:21] op_sel_hi:[1,0]
	v_cvt_pk_fp8_f32 v198, v2, v3 op_sel:[0,0,1]
	v_exp_f32_e32 v184, v184
	v_exp_f32_e32 v185, v185
	v_pk_fma_f32 v[180:181], v[98:99], v[32:33], v[8:9] op_sel_hi:[1,0,1]
	v_pk_add_f32 v[2:3], v[184:185], 1.0 op_sel_hi:[1,0]
	v_med3_f32 v180, v180, s37, v176
	v_rcp_f32_e32 v2, v2
	v_rcp_f32_e32 v3, v3
	v_med3_f32 v181, v181, s37, v176
	v_pk_mul_f32 v[2:3], v[182:183], v[2:3]
	v_pk_fma_f32 v[182:183], v[132:133], v[32:33], v[6:7] op_sel_hi:[1,0,1]
	v_pk_fma_f32 v[2:3], v[180:181], v[2:3], v[2:3]
	v_min_f32_e32 v182, 0x40e00000, v182
	v_min_f32_e32 v183, 0x40e00000, v183
	v_pk_mul_f32 v[184:185], v[182:183], s[20:21] op_sel_hi:[1,0]
	v_cvt_pk_fp8_f32 v199, v2, v3
	v_exp_f32_e32 v184, v184
	v_exp_f32_e32 v185, v185
	v_pk_fma_f32 v[32:33], v[100:101], v[32:33], v[4:5] op_sel_hi:[1,0,1]
	v_pk_fma_f32 v[180:181], v[94:95], v[30:31], v[24:25] op_sel_hi:[1,0,1]
	v_med3_f32 v32, v32, s37, v176
	v_pk_add_f32 v[2:3], v[184:185], 1.0 op_sel_hi:[1,0]
	v_med3_f32 v33, v33, s37, v176
	v_rcp_f32_e32 v2, v2
	v_rcp_f32_e32 v3, v3
	v_min_f32_e32 v180, 0x40e00000, v180
	v_min_f32_e32 v181, 0x40e00000, v181
	v_pk_mul_f32 v[2:3], v[182:183], v[2:3]
	v_pk_mul_f32 v[182:183], v[180:181], s[20:21] op_sel_hi:[1,0]
	v_pk_fma_f32 v[2:3], v[32:33], v[2:3], v[2:3]
	v_cvt_pk_fp8_f32 v199, v2, v3 op_sel:[0,0,1]
	v_exp_f32_e32 v182, v182
	v_exp_f32_e32 v183, v183
	s_mov_b32 s28, 0xc000
	v_lshl_add_u64 v[32:33], v[188:189], 0, s[28:29]
	global_store_dwordx2 v[32:33], v[198:199], off
	v_pk_add_f32 v[32:33], v[182:183], 1.0 op_sel_hi:[1,0]
	v_pk_fma_f32 v[182:183], v[62:63], v[30:31], v[16:17] op_sel_hi:[1,0,1]
	v_rcp_f32_e32 v32, v32
	v_rcp_f32_e32 v33, v33
	v_med3_f32 v182, v182, s37, v176
	v_med3_f32 v183, v183, s37, v176
	v_pk_mul_f32 v[32:33], v[180:181], v[32:33]
	v_pk_fma_f32 v[180:181], v[96:97], v[30:31], v[14:15] op_sel_hi:[1,0,1]
	v_pk_fma_f32 v[32:33], v[182:183], v[32:33], v[32:33]
	v_min_f32_e32 v180, 0x40e00000, v180
	v_min_f32_e32 v181, 0x40e00000, v181
	v_pk_mul_f32 v[184:185], v[180:181], s[20:21] op_sel_hi:[1,0]
	v_cvt_pk_fp8_f32 v200, v32, v33
	v_exp_f32_e32 v184, v184
	v_exp_f32_e32 v185, v185
	v_pk_fma_f32 v[182:183], v[64:65], v[30:31], v[12:13] op_sel_hi:[1,0,1]
	v_med3_f32 v182, v182, s37, v176
	v_pk_add_f32 v[32:33], v[184:185], 1.0 op_sel_hi:[1,0]
	v_med3_f32 v183, v183, s37, v176
	v_rcp_f32_e32 v32, v32
	v_rcp_f32_e32 v33, v33
	s_nop 0
	v_pk_mul_f32 v[32:33], v[180:181], v[32:33]
	v_pk_fma_f32 v[180:181], v[90:91], v[30:31], v[10:11] op_sel_hi:[1,0,1]
	v_pk_fma_f32 v[32:33], v[182:183], v[32:33], v[32:33]
	v_min_f32_e32 v180, 0x40e00000, v180
	v_min_f32_e32 v181, 0x40e00000, v181
	v_pk_mul_f32 v[184:185], v[180:181], s[20:21] op_sel_hi:[1,0]
	v_cvt_pk_fp8_f32 v200, v32, v33 op_sel:[0,0,1]
	v_exp_f32_e32 v184, v184
	v_exp_f32_e32 v185, v185
	v_pk_fma_f32 v[182:183], v[58:59], v[30:31], v[8:9] op_sel_hi:[1,0,1]
	v_med3_f32 v182, v182, s37, v176
	v_pk_add_f32 v[32:33], v[184:185], 1.0 op_sel_hi:[1,0]
	v_med3_f32 v183, v183, s37, v176
	v_rcp_f32_e32 v32, v32
	v_rcp_f32_e32 v33, v33
	s_nop 0
	v_pk_mul_f32 v[32:33], v[180:181], v[32:33]
	v_pk_fma_f32 v[180:181], v[92:93], v[30:31], v[6:7] op_sel_hi:[1,0,1]
	v_pk_fma_f32 v[32:33], v[182:183], v[32:33], v[32:33]
	v_min_f32_e32 v180, 0x40e00000, v180
	v_min_f32_e32 v181, 0x40e00000, v181
	v_pk_mul_f32 v[184:185], v[180:181], s[20:21] op_sel_hi:[1,0]
	v_cvt_pk_fp8_f32 v201, v32, v33
	v_exp_f32_e32 v184, v184
	v_exp_f32_e32 v185, v185
	v_pk_fma_f32 v[30:31], v[60:61], v[30:31], v[4:5] op_sel_hi:[1,0,1]
	v_med3_f32 v30, v30, s37, v176
	v_pk_add_f32 v[32:33], v[184:185], 1.0 op_sel_hi:[1,0]
	v_med3_f32 v31, v31, s37, v176
	v_rcp_f32_e32 v32, v32
	v_rcp_f32_e32 v33, v33
	s_nop 0
	v_pk_mul_f32 v[32:33], v[180:181], v[32:33]
	s_nop 0
	v_pk_fma_f32 v[30:31], v[30:31], v[32:33], v[32:33]
	v_pk_fma_f32 v[32:33], v[86:87], v[28:29], v[24:25] op_sel_hi:[1,0,1]
	v_cvt_pk_fp8_f32 v201, v30, v31 op_sel:[0,0,1]
	v_min_f32_e32 v32, 0x40e00000, v32
	v_min_f32_e32 v33, 0x40e00000, v33
	v_pk_mul_f32 v[180:181], v[32:33], s[20:21] op_sel_hi:[1,0]
	v_exp_f32_e32 v180, v180
	v_exp_f32_e32 v181, v181
	s_mov_b32 s28, 0x20000
	v_lshl_add_u64 v[2:3], v[188:189], 0, s[28:29]
	global_store_dwordx2 v[2:3], v[200:201], off
	v_pk_add_f32 v[2:3], v[180:181], 1.0 op_sel_hi:[1,0]
	v_pk_fma_f32 v[30:31], v[54:55], v[28:29], v[16:17] op_sel_hi:[1,0,1]
	v_rcp_f32_e32 v2, v2
	v_rcp_f32_e32 v3, v3
	v_med3_f32 v30, v30, s37, v176
	v_med3_f32 v31, v31, s37, v176
	v_pk_mul_f32 v[2:3], v[32:33], v[2:3]
	v_pk_fma_f32 v[32:33], v[88:89], v[28:29], v[14:15] op_sel_hi:[1,0,1]
	v_pk_fma_f32 v[2:3], v[30:31], v[2:3], v[2:3]
	v_min_f32_e32 v32, 0x40e00000, v32
	v_min_f32_e32 v33, 0x40e00000, v33
	v_pk_mul_f32 v[180:181], v[32:33], s[20:21] op_sel_hi:[1,0]
	v_cvt_pk_fp8_f32 v202, v2, v3
	v_exp_f32_e32 v180, v180
	v_exp_f32_e32 v181, v181
	v_pk_fma_f32 v[30:31], v[56:57], v[28:29], v[12:13] op_sel_hi:[1,0,1]
	v_med3_f32 v30, v30, s37, v176
	v_pk_add_f32 v[2:3], v[180:181], 1.0 op_sel_hi:[1,0]
	v_med3_f32 v31, v31, s37, v176
	v_rcp_f32_e32 v2, v2
	v_rcp_f32_e32 v3, v3
	s_nop 0
	v_pk_mul_f32 v[2:3], v[32:33], v[2:3]
	v_pk_fma_f32 v[32:33], v[82:83], v[28:29], v[10:11] op_sel_hi:[1,0,1]
	v_pk_fma_f32 v[2:3], v[30:31], v[2:3], v[2:3]
	v_min_f32_e32 v32, 0x40e00000, v32
	v_min_f32_e32 v33, 0x40e00000, v33
	v_pk_mul_f32 v[180:181], v[32:33], s[20:21] op_sel_hi:[1,0]
	v_cvt_pk_fp8_f32 v202, v2, v3 op_sel:[0,0,1]
	v_exp_f32_e32 v180, v180
	v_exp_f32_e32 v181, v181
	v_pk_fma_f32 v[30:31], v[50:51], v[28:29], v[8:9] op_sel_hi:[1,0,1]
	v_pk_add_f32 v[2:3], v[180:181], 1.0 op_sel_hi:[1,0]
	v_med3_f32 v30, v30, s37, v176
	v_rcp_f32_e32 v2, v2
	v_rcp_f32_e32 v3, v3
	v_med3_f32 v31, v31, s37, v176
	v_pk_mul_f32 v[2:3], v[32:33], v[2:3]
	v_pk_fma_f32 v[32:33], v[84:85], v[28:29], v[6:7] op_sel_hi:[1,0,1]
	v_pk_fma_f32 v[2:3], v[30:31], v[2:3], v[2:3]
	v_min_f32_e32 v32, 0x40e00000, v32
	v_min_f32_e32 v33, 0x40e00000, v33
	v_pk_mul_f32 v[180:181], v[32:33], s[20:21] op_sel_hi:[1,0]
	v_cvt_pk_fp8_f32 v203, v2, v3
	v_exp_f32_e32 v180, v180
	v_exp_f32_e32 v181, v181
	v_pk_fma_f32 v[28:29], v[52:53], v[28:29], v[4:5] op_sel_hi:[1,0,1]
	v_pk_fma_f32 v[30:31], v[78:79], v[26:27], v[24:25] op_sel_hi:[1,0,1]
	v_med3_f32 v28, v28, s37, v176
	v_pk_add_f32 v[2:3], v[180:181], 1.0 op_sel_hi:[1,0]
	v_med3_f32 v29, v29, s37, v176
	v_rcp_f32_e32 v2, v2
	v_rcp_f32_e32 v3, v3
	v_min_f32_e32 v30, 0x40e00000, v30
	v_min_f32_e32 v31, 0x40e00000, v31
	v_pk_mul_f32 v[2:3], v[32:33], v[2:3]
	v_pk_mul_f32 v[32:33], v[30:31], s[20:21] op_sel_hi:[1,0]
	v_pk_fma_f32 v[2:3], v[28:29], v[2:3], v[2:3]
	v_cvt_pk_fp8_f32 v203, v2, v3 op_sel:[0,0,1]
	v_exp_f32_e32 v32, v32
	v_exp_f32_e32 v33, v33
	s_mov_b32 s28, 0x24000
	v_lshl_add_u64 v[28:29], v[188:189], 0, s[28:29]
	global_store_dwordx2 v[28:29], v[202:203], off
	v_pk_add_f32 v[2:3], v[32:33], 1.0 op_sel_hi:[1,0]
	v_pk_fma_f32 v[28:29], v[46:47], v[26:27], v[16:17] op_sel_hi:[1,0,1]
	v_rcp_f32_e32 v2, v2
	v_rcp_f32_e32 v3, v3
	v_med3_f32 v28, v28, s37, v176
	v_med3_f32 v29, v29, s37, v176
	v_pk_mul_f32 v[2:3], v[30:31], v[2:3]
	v_pk_fma_f32 v[30:31], v[80:81], v[26:27], v[14:15] op_sel_hi:[1,0,1]
	v_pk_fma_f32 v[2:3], v[28:29], v[2:3], v[2:3]
	v_min_f32_e32 v30, 0x40e00000, v30
	v_min_f32_e32 v31, 0x40e00000, v31
	v_pk_mul_f32 v[32:33], v[30:31], s[20:21] op_sel_hi:[1,0]
	v_cvt_pk_fp8_f32 v204, v2, v3
	v_exp_f32_e32 v32, v32
	v_exp_f32_e32 v33, v33
	v_pk_fma_f32 v[28:29], v[48:49], v[26:27], v[12:13] op_sel_hi:[1,0,1]
	v_med3_f32 v28, v28, s37, v176
	v_pk_add_f32 v[2:3], v[32:33], 1.0 op_sel_hi:[1,0]
	v_med3_f32 v29, v29, s37, v176
	v_rcp_f32_e32 v2, v2
	v_rcp_f32_e32 v3, v3
	s_nop 0
	v_pk_mul_f32 v[2:3], v[30:31], v[2:3]
	v_pk_fma_f32 v[30:31], v[74:75], v[26:27], v[10:11] op_sel_hi:[1,0,1]
	v_pk_fma_f32 v[2:3], v[28:29], v[2:3], v[2:3]
	v_min_f32_e32 v30, 0x40e00000, v30
	v_min_f32_e32 v31, 0x40e00000, v31
	v_pk_mul_f32 v[32:33], v[30:31], s[20:21] op_sel_hi:[1,0]
	v_cvt_pk_fp8_f32 v204, v2, v3 op_sel:[0,0,1]
	v_exp_f32_e32 v32, v32
	v_exp_f32_e32 v33, v33
	v_pk_fma_f32 v[28:29], v[42:43], v[26:27], v[8:9] op_sel_hi:[1,0,1]
	v_pk_fma_f32 v[24:25], v[70:71], v[22:23], v[24:25] op_sel_hi:[1,0,1]
	v_med3_f32 v28, v28, s37, v176
	v_pk_add_f32 v[2:3], v[32:33], 1.0 op_sel_hi:[1,0]
	v_med3_f32 v29, v29, s37, v176
	v_rcp_f32_e32 v2, v2
	v_rcp_f32_e32 v3, v3
	v_min_f32_e32 v24, 0x40e00000, v24
	v_min_f32_e32 v25, 0x40e00000, v25
	v_pk_fma_f32 v[14:15], v[72:73], v[22:23], v[14:15] op_sel_hi:[1,0,1]
	v_pk_mul_f32 v[2:3], v[30:31], v[2:3]
	v_pk_fma_f32 v[30:31], v[76:77], v[26:27], v[6:7] op_sel_hi:[1,0,1]
	v_pk_fma_f32 v[2:3], v[28:29], v[2:3], v[2:3]
	v_min_f32_e32 v30, 0x40e00000, v30
	v_min_f32_e32 v31, 0x40e00000, v31
	v_pk_mul_f32 v[32:33], v[30:31], s[20:21] op_sel_hi:[1,0]
	v_exp_f32_e32 v32, v32
	v_exp_f32_e32 v33, v33
	v_cvt_pk_fp8_f32 v205, v2, v3
	v_pk_fma_f32 v[26:27], v[44:45], v[26:27], v[4:5] op_sel_hi:[1,0,1]
	v_min_f32_e32 v14, 0x40e00000, v14
	v_pk_add_f32 v[2:3], v[32:33], 1.0 op_sel_hi:[1,0]
	v_med3_f32 v26, v26, s37, v176
	v_rcp_f32_e32 v2, v2
	v_rcp_f32_e32 v3, v3
	v_med3_f32 v27, v27, s37, v176
	v_min_f32_e32 v15, 0x40e00000, v15
	v_pk_fma_f32 v[16:17], v[38:39], v[22:23], v[16:17] op_sel_hi:[1,0,1]
	v_pk_mul_f32 v[2:3], v[30:31], v[2:3]
	v_med3_f32 v16, v16, s37, v176
	v_pk_fma_f32 v[2:3], v[26:27], v[2:3], v[2:3]
	v_cvt_pk_fp8_f32 v205, v2, v3 op_sel:[0,0,1]
	v_pk_mul_f32 v[28:29], v[24:25], s[20:21] op_sel_hi:[1,0]
	v_exp_f32_e32 v28, v28
	v_exp_f32_e32 v29, v29
	s_mov_b32 s28, 0x28000
	v_lshl_add_u64 v[26:27], v[188:189], 0, s[28:29]
	global_store_dwordx2 v[26:27], v[204:205], off
	v_pk_add_f32 v[2:3], v[28:29], 1.0 op_sel_hi:[1,0]
	v_med3_f32 v17, v17, s37, v176
	v_rcp_f32_e32 v2, v2
	v_rcp_f32_e32 v3, v3
	v_pk_fma_f32 v[10:11], v[66:67], v[22:23], v[10:11] op_sel_hi:[1,0,1]
	v_pk_fma_f32 v[12:13], v[40:41], v[22:23], v[12:13] op_sel_hi:[1,0,1]
	v_min_f32_e32 v10, 0x40e00000, v10
	v_pk_mul_f32 v[2:3], v[24:25], v[2:3]
	v_pk_mul_f32 v[24:25], v[14:15], s[20:21] op_sel_hi:[1,0]
	v_pk_fma_f32 v[2:3], v[16:17], v[2:3], v[2:3]
	v_exp_f32_e32 v24, v24
	v_exp_f32_e32 v25, v25
	v_cvt_pk_fp8_f32 v206, v2, v3
	v_min_f32_e32 v11, 0x40e00000, v11
	v_pk_add_f32 v[2:3], v[24:25], 1.0 op_sel_hi:[1,0]
	v_med3_f32 v12, v12, s37, v176
	v_rcp_f32_e32 v2, v2
	v_rcp_f32_e32 v3, v3
	v_med3_f32 v13, v13, s37, v176
	v_pk_fma_f32 v[6:7], v[68:69], v[22:23], v[6:7] op_sel_hi:[1,0,1]
	v_pk_fma_f32 v[8:9], v[34:35], v[22:23], v[8:9] op_sel_hi:[1,0,1]
	v_pk_mul_f32 v[2:3], v[14:15], v[2:3]
	v_pk_mul_f32 v[14:15], v[10:11], s[20:21] op_sel_hi:[1,0]
	v_pk_fma_f32 v[2:3], v[12:13], v[2:3], v[2:3]
	v_exp_f32_e32 v14, v14
	v_exp_f32_e32 v15, v15
	v_cvt_pk_fp8_f32 v206, v2, v3 op_sel:[0,0,1]
	v_min_f32_e32 v6, 0x40e00000, v6
	v_pk_add_f32 v[2:3], v[14:15], 1.0 op_sel_hi:[1,0]
	v_min_f32_e32 v7, 0x40e00000, v7
	v_rcp_f32_e32 v2, v2
	v_rcp_f32_e32 v3, v3
	v_med3_f32 v8, v8, s37, v176
	v_med3_f32 v9, v9, s37, v176
	v_pk_fma_f32 v[4:5], v[36:37], v[22:23], v[4:5] op_sel_hi:[1,0,1]
	v_pk_mul_f32 v[2:3], v[10:11], v[2:3]
	v_pk_mul_f32 v[10:11], v[6:7], s[20:21] op_sel_hi:[1,0]
	v_pk_fma_f32 v[2:3], v[8:9], v[2:3], v[2:3]
	v_exp_f32_e32 v10, v10
	v_exp_f32_e32 v11, v11
	v_cvt_pk_fp8_f32 v207, v2, v3
	v_med3_f32 v4, v4, s37, v176
	v_pk_add_f32 v[2:3], v[10:11], 1.0 op_sel_hi:[1,0]
	v_med3_f32 v5, v5, s37, v176
	v_rcp_f32_e32 v2, v2
	v_rcp_f32_e32 v3, v3
	s_nop 0
	v_pk_mul_f32 v[2:3], v[6:7], v[2:3]
	s_nop 0
	v_pk_fma_f32 v[2:3], v[4:5], v[2:3], v[2:3]
	v_cvt_pk_fp8_f32 v207, v2, v3 op_sel:[0,0,1]
	s_mov_b32 s28, 0x2c000
	v_lshl_add_u64 v[4:5], v[188:189], 0, s[28:29]
	global_store_dwordx2 v[4:5], v[206:207], off
	s_cbranch_vccnz .LBB0_1920
	s_andn2_b64 vcc, exec, s[0:1]
	s_cbranch_vccnz .LBB0_1919
	s_barrier
